# adds non-temporal hint on the residual-stream stores of the expert-combine norm pass
# speedup vs baseline: 1.0320x; 1.0074x over previous
.LBB0_54:
	v_pk_mul_f32 v[82:83], v[80:81], v[80:81]
	v_pk_mul_f32 v[84:85], v[78:79], v[78:79]
	v_add_f32_e32 v82, v82, v83
	v_add_f32_e32 v82, v84, v82
	v_pk_mul_f32 v[86:87], v[76:77], v[76:77]
	v_add_f32_e32 v82, v85, v82
	v_add_f32_e32 v82, v86, v82
	v_pk_mul_f32 v[88:89], v[74:75], v[74:75]
	v_add_f32_e32 v82, v87, v82
	v_add_f32_e32 v82, v88, v82
	v_pk_mul_f32 v[90:91], v[72:73], v[72:73]
	v_add_f32_e32 v82, v89, v82
	v_add_f32_e32 v82, v90, v82
	v_pk_mul_f32 v[92:93], v[70:71], v[70:71]
	v_add_f32_e32 v82, v91, v82
	v_add_f32_e32 v82, v92, v82
	v_pk_mul_f32 v[100:101], v[68:69], v[68:69]
	v_add_f32_e32 v82, v93, v82
	v_add_f32_e32 v82, v100, v82
	v_pk_mul_f32 v[102:103], v[66:67], v[66:67]
	v_add_f32_e32 v82, v101, v82
	v_add_f32_e32 v82, v102, v82
	v_add_f32_e32 v82, v103, v82
	ds_bpermute_b32 v83, v48, v82
	s_mov_b32 s0, 0xf800000
	v_cvt_pk_bf16_f32 v86, v72, v73
	v_cvt_pk_bf16_f32 v87, v70, v71
	s_waitcnt lgkmcnt(0)
	v_add_f32_e32 v82, v82, v83
	ds_bpermute_b32 v83, v95, v82
	s_waitcnt lgkmcnt(0)
	v_add_f32_e32 v82, v82, v83
	ds_bpermute_b32 v83, v96, v82
	s_waitcnt lgkmcnt(0)
	v_add_f32_e32 v82, v82, v83
	ds_bpermute_b32 v83, v97, v82
	s_waitcnt lgkmcnt(0)
	v_add_f32_e32 v84, v82, v83
	ds_bpermute_b32 v85, v98, v84
	v_cvt_pk_bf16_f32 v82, v80, v81
	v_cvt_pk_bf16_f32 v83, v78, v79
	s_waitcnt lgkmcnt(0)
	v_add_f32_e32 v88, v84, v85
	ds_bpermute_b32 v89, v99, v88
	v_cvt_pk_bf16_f32 v84, v76, v77
	v_cvt_pk_bf16_f32 v85, v74, v75
	global_store_dwordx4 v[64:65], v[82:85], off nt
	s_waitcnt lgkmcnt(0)
	v_add_f32_e32 v88, v88, v89
	v_fmamk_f32 v88, v88, 0x3a800000, v229
	v_mul_f32_e32 v89, 0x4f800000, v88
	v_cmp_gt_f32_e32 vcc, s0, v88
	s_nop 1
	v_cndmask_b32_e32 v90, v88, v89, vcc
	v_sqrt_f32_e32 v91, v90
	v_cvt_pk_bf16_f32 v88, v68, v69
	v_cvt_pk_bf16_f32 v89, v66, v67
	global_store_dwordx4 v[64:65], v[86:89], off offset:1024 nt
	v_add_u32_e32 v82, -1, v91
	v_add_u32_e32 v83, 1, v91
	v_fma_f32 v84, -v82, v91, v90
	v_fma_f32 v85, -v83, v91, v90
	v_cmp_ge_f32_e64 s[36:37], 0, v84
	s_nop 1
	v_cndmask_b32_e64 v82, v91, v82, s[36:37]
	v_cmp_lt_f32_e64 s[36:37], 0, v85
	s_nop 1
	v_cndmask_b32_e64 v82, v82, v83, s[36:37]
	v_mul_f32_e32 v83, 0x37800000, v82
	v_cndmask_b32_e32 v82, v82, v83, vcc
	v_cmp_class_f32_e32 vcc, v90, v230
	s_nop 1
	v_cndmask_b32_e32 v82, v82, v90, vcc
	v_div_scale_f32 v83, s[0:1], v82, v82, 1.0
	v_rcp_f32_e32 v84, v83
	v_div_scale_f32 v64, vcc, 1.0, v82, 1.0
	v_fma_f32 v65, -v83, v84, 1.0
	v_fmac_f32_e32 v84, v65, v84
	v_mul_f32_e32 v65, v64, v84
	v_fma_f32 v85, -v83, v65, v64
	v_fmac_f32_e32 v65, v85, v84
	v_fma_f32 v64, -v83, v65, v64
	v_div_fmas_f32 v64, v64, v84, v65
	v_div_fixup_f32 v64, v64, v82, 1.0
	s_and_saveexec_b64 s[0:1], s[34:35]
	s_cbranch_execz .LBB0_56
	s_lshl_b64 s[4:5], s[42:43], 2
	s_add_u32 s4, s6, s4
	s_addc_u32 s5, s7, s5
	global_store_dword v49, v64, s[4:5]
.LBB0_56:
	s_or_b64 exec, exec, s[0:1]
	v_mul_f32_e32 v86, 0x41800000, v64
	v_mul_f32_e32 v64, v80, v86
	v_mul_f32_e32 v65, v81, v86
	v_med3_f32 v80, v64, s11, v232
	v_med3_f32 v65, v65, s11, v232
	v_mov_b32_e32 v64, v49
	v_cvt_pk_fp8_f32 v64, v80, v65
	v_mul_f32_e32 v78, v78, v86
	v_mul_f32_e32 v65, v79, v86
	v_med3_f32 v78, v78, s11, v232
	v_med3_f32 v65, v65, s11, v232
	v_cvt_pk_fp8_f32 v64, v78, v65 op_sel:[0,0,1]
	v_mul_f32_e32 v65, v76, v86
	v_mul_f32_e32 v76, v77, v86
	v_med3_f32 v77, v65, s11, v232
	v_med3_f32 v76, v76, s11, v232
	v_mov_b32_e32 v65, v49
	v_cvt_pk_fp8_f32 v65, v77, v76
	v_mul_f32_e32 v72, v72, v86
	v_mul_f32_e32 v73, v73, v86
	v_mul_f32_e32 v87, v70, v86
	v_mul_f32_e32 v88, v71, v86
	v_pk_mul_f32 v[70:71], v[62:63], v[62:63]
	v_mul_f32_e32 v74, v74, v86
	v_mul_f32_e32 v75, v75, v86
	v_med3_f32 v89, v72, s11, v232
	v_med3_f32 v90, v73, s11, v232
	v_pk_mul_f32 v[72:73], v[60:61], v[60:61]
	v_add_f32_e32 v70, v70, v71
	v_med3_f32 v74, v74, s11, v232
	v_med3_f32 v75, v75, s11, v232
	v_add_f32_e32 v70, v72, v70
	v_cvt_pk_fp8_f32 v65, v74, v75 op_sel:[0,0,1]
	v_pk_mul_f32 v[74:75], v[58:59], v[58:59]
	v_add_f32_e32 v70, v73, v70
	v_add_f32_e32 v70, v74, v70
	v_pk_mul_f32 v[76:77], v[56:57], v[56:57]
	v_add_f32_e32 v70, v75, v70
	v_add_f32_e32 v70, v76, v70
	v_pk_mul_f32 v[78:79], v[54:55], v[54:55]
	v_add_f32_e32 v70, v77, v70
	v_add_f32_e32 v70, v78, v70
	v_pk_mul_f32 v[80:81], v[52:53], v[52:53]
	v_add_f32_e32 v70, v79, v70
	v_add_f32_e32 v70, v80, v70
	v_pk_mul_f32 v[82:83], v[50:51], v[50:51]
	v_add_f32_e32 v70, v81, v70
	v_add_f32_e32 v70, v82, v70
	v_pk_mul_f32 v[84:85], v[46:47], v[46:47]
	v_add_f32_e32 v70, v83, v70
	v_add_f32_e32 v70, v84, v70
	v_add_f32_e32 v71, v85, v70
	ds_bpermute_b32 v72, v48, v71
	v_mov_b32_e32 v70, v49
	v_cvt_pk_fp8_f32 v70, v89, v90
	v_med3_f32 v73, v87, s11, v232
	v_med3_f32 v74, v88, s11, v232
	s_waitcnt lgkmcnt(0)
	v_add_f32_e32 v71, v71, v72
	ds_bpermute_b32 v72, v95, v71
	v_cvt_pk_fp8_f32 v70, v73, v74 op_sel:[0,0,1]
	v_mul_f32_e32 v68, v68, v86
	v_mul_f32_e32 v69, v69, v86
	v_med3_f32 v68, v68, s11, v232
	s_waitcnt lgkmcnt(0)
	v_add_f32_e32 v72, v71, v72
	ds_bpermute_b32 v73, v96, v72
	v_med3_f32 v69, v69, s11, v232
	v_mov_b32_e32 v71, v49
	v_cvt_pk_fp8_f32 v71, v68, v69
	v_mul_f32_e32 v66, v66, v86
	s_waitcnt lgkmcnt(0)
	v_add_f32_e32 v68, v72, v73
	ds_bpermute_b32 v69, v97, v68
	v_mul_f32_e32 v67, v67, v86
	v_med3_f32 v66, v66, s11, v232
	v_med3_f32 v67, v67, s11, v232
	s_lshl_b64 s[0:1], s[42:43], 10
	s_waitcnt lgkmcnt(0)
	v_add_f32_e32 v68, v68, v69
	ds_bpermute_b32 v69, v98, v68
	v_cvt_pk_fp8_f32 v71, v66, v67 op_sel:[0,0,1]
	v_lshl_add_u64 v[66:67], v[6:7], 0, s[0:1]
	s_mov_b32 s0, 0xf800000
	global_store_dwordx2 v[66:67], v[64:65], off
	global_store_dwordx2 v[66:67], v[70:71], off offset:512
	s_waitcnt lgkmcnt(0)
	v_add_f32_e32 v68, v68, v69
	ds_bpermute_b32 v69, v99, v68
	v_cvt_pk_bf16_f32 v64, v62, v63
	v_cvt_pk_bf16_f32 v65, v60, v61
	v_cvt_pk_bf16_f32 v66, v58, v59
	v_cvt_pk_bf16_f32 v67, v56, v57
	s_waitcnt lgkmcnt(0)
	v_add_f32_e32 v68, v68, v69
	v_fmamk_f32 v68, v68, 0x3a800000, v229
	v_mul_f32_e32 v69, 0x4f800000, v68
	v_cmp_gt_f32_e32 vcc, s0, v68
	global_store_dwordx4 v[44:45], v[64:67], off nt
	s_nop 0
	v_cndmask_b32_e32 v68, v68, v69, vcc
	v_sqrt_f32_e32 v69, v68
	v_cvt_pk_bf16_f32 v64, v54, v55
	v_cvt_pk_bf16_f32 v65, v52, v53
	v_add_u32_e32 v66, -1, v69
	v_fma_f32 v67, -v66, v69, v68
	v_cmp_ge_f32_e64 s[36:37], 0, v67
	v_add_u32_e32 v67, 1, v69
	s_nop 0
	v_cndmask_b32_e64 v66, v69, v66, s[36:37]
	v_fma_f32 v69, -v67, v69, v68
	v_cmp_lt_f32_e64 s[36:37], 0, v69
	s_nop 1
	v_cndmask_b32_e64 v66, v66, v67, s[36:37]
	v_mul_f32_e32 v67, 0x37800000, v66
	v_cndmask_b32_e32 v66, v66, v67, vcc
	v_cmp_class_f32_e32 vcc, v68, v230
	v_cvt_pk_bf16_f32 v67, v46, v47
	s_nop 0
	v_cndmask_b32_e32 v68, v66, v68, vcc
	v_div_scale_f32 v69, s[0:1], v68, v68, 1.0
	v_rcp_f32_e32 v70, v69
	v_cvt_pk_bf16_f32 v66, v50, v51
	global_store_dwordx4 v[44:45], v[64:67], off offset:1024 nt
	v_fma_f32 v44, -v69, v70, 1.0
	v_fmac_f32_e32 v70, v44, v70
	v_div_scale_f32 v44, vcc, 1.0, v68, 1.0
	v_mul_f32_e32 v45, v44, v70
	v_fma_f32 v64, -v69, v45, v44
	v_fmac_f32_e32 v45, v64, v70
	v_fma_f32 v44, -v69, v45, v44
	v_div_fmas_f32 v44, v44, v70, v45
	v_div_fixup_f32 v44, v44, v68, 1.0
	s_and_saveexec_b64 s[0:1], s[34:35]
	s_cbranch_execz .LBB0_58
	s_lshl_b64 s[4:5], s[48:49], 2
	s_add_u32 s4, s6, s4
	s_addc_u32 s5, s7, s5
	global_store_dword v49, v44, s[4:5]
.LBB0_58:
	s_or_b64 exec, exec, s[0:1]
	v_mul_f32_e32 v68, 0x41800000, v44
	v_mul_f32_e32 v44, v62, v68
	v_mul_f32_e32 v45, v63, v68
	v_med3_f32 v62, v44, s11, v232
	v_med3_f32 v45, v45, s11, v232
	v_mov_b32_e32 v44, v49
	v_cvt_pk_fp8_f32 v44, v62, v45
	v_mul_f32_e32 v60, v60, v68
	v_mul_f32_e32 v45, v61, v68
	v_med3_f32 v60, v60, s11, v232
	v_med3_f32 v45, v45, s11, v232
	v_cvt_pk_fp8_f32 v44, v60, v45 op_sel:[0,0,1]
	v_mul_f32_e32 v45, v58, v68
	v_mul_f32_e32 v58, v59, v68
	v_med3_f32 v59, v45, s11, v232
	v_med3_f32 v58, v58, s11, v232
	v_mov_b32_e32 v45, v49
	v_cvt_pk_fp8_f32 v45, v59, v58
	v_mul_f32_e32 v54, v54, v68
	v_mul_f32_e32 v55, v55, v68
	v_mul_f32_e32 v69, v52, v68
	v_mul_f32_e32 v70, v53, v68
	v_pk_mul_f32 v[52:53], v[42:43], v[42:43]
	v_mul_f32_e32 v56, v56, v68
	v_mul_f32_e32 v57, v57, v68
	v_med3_f32 v71, v54, s11, v232
	v_med3_f32 v72, v55, s11, v232
	v_pk_mul_f32 v[54:55], v[40:41], v[40:41]
	v_add_f32_e32 v52, v52, v53
	v_med3_f32 v56, v56, s11, v232
	v_med3_f32 v57, v57, s11, v232
	v_add_f32_e32 v52, v52, v54
	v_cvt_pk_fp8_f32 v45, v56, v57 op_sel:[0,0,1]
	v_pk_mul_f32 v[56:57], v[38:39], v[38:39]
	v_add_f32_e32 v52, v55, v52
	v_add_f32_e32 v52, v56, v52
	v_pk_mul_f32 v[58:59], v[36:37], v[36:37]
	v_add_f32_e32 v52, v57, v52
	v_add_f32_e32 v52, v58, v52
	v_pk_mul_f32 v[60:61], v[32:33], v[32:33]
	v_add_f32_e32 v52, v59, v52
	v_add_f32_e32 v52, v60, v52
	v_pk_mul_f32 v[62:63], v[34:35], v[34:35]
	v_add_f32_e32 v52, v61, v52
	v_add_f32_e32 v52, v62, v52
	v_pk_mul_f32 v[64:65], v[28:29], v[28:29]
	v_add_f32_e32 v52, v63, v52
	v_add_f32_e32 v52, v64, v52
	v_pk_mul_f32 v[66:67], v[26:27], v[26:27]
	v_add_f32_e32 v52, v65, v52
	v_add_f32_e32 v52, v66, v52
	v_add_f32_e32 v53, v67, v52
	ds_bpermute_b32 v54, v48, v53
	v_mov_b32_e32 v52, v49
	v_cvt_pk_fp8_f32 v52, v71, v72
	v_med3_f32 v55, v69, s11, v232
	v_med3_f32 v56, v70, s11, v232
	s_waitcnt lgkmcnt(0)
	v_add_f32_e32 v53, v53, v54
	ds_bpermute_b32 v54, v95, v53
	v_cvt_pk_fp8_f32 v52, v55, v56 op_sel:[0,0,1]
	v_mul_f32_e32 v50, v50, v68
	v_mul_f32_e32 v51, v51, v68
	v_med3_f32 v50, v50, s11, v232
	s_waitcnt lgkmcnt(0)
	v_add_f32_e32 v54, v53, v54
	ds_bpermute_b32 v55, v96, v54
	v_med3_f32 v51, v51, s11, v232
	v_mov_b32_e32 v53, v49
	v_cvt_pk_fp8_f32 v53, v50, v51
	v_mul_f32_e32 v46, v46, v68
	s_waitcnt lgkmcnt(0)
	v_add_f32_e32 v50, v54, v55
	ds_bpermute_b32 v51, v97, v50
	v_mul_f32_e32 v47, v47, v68
	v_med3_f32 v46, v46, s11, v232
	v_med3_f32 v47, v47, s11, v232
	s_lshl_b64 s[0:1], s[48:49], 10
	s_waitcnt lgkmcnt(0)
	v_add_f32_e32 v50, v50, v51
	ds_bpermute_b32 v51, v98, v50
	v_cvt_pk_fp8_f32 v53, v46, v47 op_sel:[0,0,1]
	v_lshl_add_u64 v[46:47], v[6:7], 0, s[0:1]
	s_mov_b32 s0, 0xf800000
	global_store_dwordx2 v[46:47], v[44:45], off
	global_store_dwordx2 v[46:47], v[52:53], off offset:512
	s_waitcnt lgkmcnt(0)
	v_add_f32_e32 v50, v50, v51
	ds_bpermute_b32 v51, v99, v50
	v_cvt_pk_bf16_f32 v44, v42, v43
	v_cvt_pk_bf16_f32 v45, v40, v41
	v_cvt_pk_bf16_f32 v46, v38, v39
	v_cvt_pk_bf16_f32 v47, v36, v37
	s_waitcnt lgkmcnt(0)
	v_add_f32_e32 v50, v50, v51
	v_fmamk_f32 v50, v50, 0x3a800000, v229
	v_mul_f32_e32 v51, 0x4f800000, v50
	v_cmp_gt_f32_e32 vcc, s0, v50
	global_store_dwordx4 v[30:31], v[44:47], off nt
	s_nop 0
	v_cndmask_b32_e32 v50, v50, v51, vcc
	v_sqrt_f32_e32 v51, v50
	v_cvt_pk_bf16_f32 v44, v32, v33
	v_cvt_pk_bf16_f32 v45, v34, v35
	v_add_u32_e32 v46, -1, v51
	v_fma_f32 v47, -v46, v51, v50
	v_cmp_ge_f32_e64 s[36:37], 0, v47
	v_add_u32_e32 v47, 1, v51
	s_nop 0
	v_cndmask_b32_e64 v46, v51, v46, s[36:37]
	v_fma_f32 v51, -v47, v51, v50
	v_cmp_lt_f32_e64 s[36:37], 0, v51
	s_nop 1
	v_cndmask_b32_e64 v46, v46, v47, s[36:37]
	v_mul_f32_e32 v47, 0x37800000, v46
	v_cndmask_b32_e32 v46, v46, v47, vcc
	v_cmp_class_f32_e32 vcc, v50, v230
	v_cvt_pk_bf16_f32 v47, v26, v27
	s_nop 0
	v_cndmask_b32_e32 v50, v46, v50, vcc
	v_div_scale_f32 v51, s[0:1], v50, v50, 1.0
	v_rcp_f32_e32 v52, v51
	v_cvt_pk_bf16_f32 v46, v28, v29
	global_store_dwordx4 v[30:31], v[44:47], off offset:1024 nt
	v_fma_f32 v30, -v51, v52, 1.0
	v_fmac_f32_e32 v52, v30, v52
	v_div_scale_f32 v30, vcc, 1.0, v50, 1.0
	v_mul_f32_e32 v31, v30, v52
	v_fma_f32 v44, -v51, v31, v30
	v_fmac_f32_e32 v31, v44, v52
	v_fma_f32 v30, -v51, v31, v30
	v_div_fmas_f32 v30, v30, v52, v31
	v_div_fixup_f32 v30, v30, v50, 1.0
	s_and_saveexec_b64 s[0:1], s[34:35]
	s_cbranch_execz .LBB0_60
	s_lshl_b64 s[4:5], s[46:47], 2
	s_add_u32 s4, s6, s4
	s_addc_u32 s5, s7, s5
	global_store_dword v49, v30, s[4:5]
.LBB0_60:
	s_or_b64 exec, exec, s[0:1]
	v_mul_f32_e32 v50, 0x41800000, v30
	v_mul_f32_e32 v30, v42, v50
	v_mul_f32_e32 v31, v43, v50
	v_med3_f32 v42, v30, s11, v232
	v_med3_f32 v31, v31, s11, v232
	v_mov_b32_e32 v30, v49
	v_cvt_pk_fp8_f32 v30, v42, v31
	v_mul_f32_e32 v40, v40, v50
	v_mul_f32_e32 v31, v41, v50
	v_med3_f32 v40, v40, s11, v232
	v_med3_f32 v31, v31, s11, v232
	v_cvt_pk_fp8_f32 v30, v40, v31 op_sel:[0,0,1]
	v_mul_f32_e32 v31, v38, v50
	v_mul_f32_e32 v38, v39, v50
	v_med3_f32 v39, v31, s11, v232
	v_med3_f32 v38, v38, s11, v232
	v_mov_b32_e32 v31, v49
	v_cvt_pk_fp8_f32 v31, v39, v38
	v_mul_f32_e32 v32, v32, v50
	v_mul_f32_e32 v33, v33, v50
	v_med3_f32 v53, v32, s11, v232
	v_med3_f32 v54, v33, s11, v232
	v_pk_mul_f32 v[32:33], v[24:25], v[24:25]
	v_mul_f32_e32 v36, v36, v50
	v_mul_f32_e32 v37, v37, v50
	v_mul_f32_e32 v51, v34, v50
	v_mul_f32_e32 v52, v35, v50
	v_pk_mul_f32 v[34:35], v[22:23], v[22:23]
	v_add_f32_e32 v32, v32, v33
	v_med3_f32 v36, v36, s11, v232
	v_med3_f32 v37, v37, s11, v232
	v_add_f32_e32 v32, v32, v34
	v_cvt_pk_fp8_f32 v31, v36, v37 op_sel:[0,0,1]
	v_pk_mul_f32 v[36:37], v[20:21], v[20:21]
	v_add_f32_e32 v32, v35, v32
	v_add_f32_e32 v32, v36, v32
	v_pk_mul_f32 v[38:39], v[18:19], v[18:19]
	v_add_f32_e32 v32, v37, v32
	v_add_f32_e32 v32, v38, v32
	v_pk_mul_f32 v[40:41], v[16:17], v[16:17]
	v_add_f32_e32 v32, v39, v32
	v_add_f32_e32 v32, v40, v32
	v_pk_mul_f32 v[42:43], v[14:15], v[14:15]
	v_add_f32_e32 v32, v41, v32
	v_add_f32_e32 v32, v42, v32
	v_pk_mul_f32 v[44:45], v[12:13], v[12:13]
	v_add_f32_e32 v32, v43, v32
	v_add_f32_e32 v32, v44, v32
	v_pk_mul_f32 v[46:47], v[10:11], v[10:11]
	v_add_f32_e32 v32, v45, v32
	v_add_f32_e32 v32, v46, v32
	v_add_f32_e32 v33, v47, v32
	ds_bpermute_b32 v34, v48, v33
	v_mov_b32_e32 v32, v49
	v_cvt_pk_fp8_f32 v32, v53, v54
	v_med3_f32 v35, v51, s11, v232
	v_med3_f32 v36, v52, s11, v232
	s_waitcnt lgkmcnt(0)
	v_add_f32_e32 v33, v33, v34
	ds_bpermute_b32 v34, v95, v33
	v_cvt_pk_fp8_f32 v32, v35, v36 op_sel:[0,0,1]
	v_mul_f32_e32 v28, v28, v50
	v_mul_f32_e32 v29, v29, v50
	v_med3_f32 v28, v28, s11, v232
	s_waitcnt lgkmcnt(0)
	v_add_f32_e32 v34, v33, v34
	ds_bpermute_b32 v35, v96, v34
	v_med3_f32 v29, v29, s11, v232
	v_mov_b32_e32 v33, v49
	v_cvt_pk_fp8_f32 v33, v28, v29
	v_mul_f32_e32 v26, v26, v50
	s_waitcnt lgkmcnt(0)
	v_add_f32_e32 v28, v34, v35
	ds_bpermute_b32 v29, v97, v28
	v_mul_f32_e32 v27, v27, v50
	v_med3_f32 v26, v26, s11, v232
	v_med3_f32 v27, v27, s11, v232
	v_cvt_pk_fp8_f32 v33, v26, v27 op_sel:[0,0,1]
	s_waitcnt lgkmcnt(0)
	v_add_f32_e32 v28, v28, v29
	ds_bpermute_b32 v29, v98, v28
	s_lshl_b64 s[0:1], s[46:47], 10
	v_lshl_add_u64 v[26:27], v[6:7], 0, s[0:1]
	global_store_dwordx2 v[26:27], v[30:31], off
	global_store_dwordx2 v[26:27], v[32:33], off offset:512
	s_mov_b32 s0, 0xf800000
	s_waitcnt lgkmcnt(0)
	v_add_f32_e32 v30, v28, v29
	ds_bpermute_b32 v31, v99, v30
	v_cvt_pk_bf16_f32 v26, v24, v25
	v_cvt_pk_bf16_f32 v27, v22, v23
	v_cvt_pk_bf16_f32 v28, v20, v21
	v_cvt_pk_bf16_f32 v29, v18, v19
	s_waitcnt lgkmcnt(0)
	v_add_f32_e32 v30, v30, v31
	v_fmamk_f32 v30, v30, 0x3a800000, v229
	v_mul_f32_e32 v31, 0x4f800000, v30
	v_cmp_gt_f32_e32 vcc, s0, v30
	global_store_dwordx4 v[8:9], v[26:29], off nt
	s_nop 0
	v_cndmask_b32_e32 v30, v30, v31, vcc
	v_sqrt_f32_e32 v31, v30
	v_cvt_pk_bf16_f32 v26, v16, v17
	v_cvt_pk_bf16_f32 v27, v14, v15
	v_add_u32_e32 v28, -1, v31
	v_fma_f32 v29, -v28, v31, v30
	v_cmp_ge_f32_e64 s[36:37], 0, v29
	v_add_u32_e32 v29, 1, v31
	s_nop 0
	v_cndmask_b32_e64 v28, v31, v28, s[36:37]
	v_fma_f32 v31, -v29, v31, v30
	v_cmp_lt_f32_e64 s[36:37], 0, v31
	s_nop 1
	v_cndmask_b32_e64 v28, v28, v29, s[36:37]
	v_mul_f32_e32 v29, 0x37800000, v28
	v_cndmask_b32_e32 v28, v28, v29, vcc
	v_cmp_class_f32_e32 vcc, v30, v230
	v_cvt_pk_bf16_f32 v29, v10, v11
	s_nop 0
	v_cndmask_b32_e32 v30, v28, v30, vcc
	v_div_scale_f32 v31, s[0:1], v30, v30, 1.0
	v_rcp_f32_e32 v32, v31
	v_cvt_pk_bf16_f32 v28, v12, v13
	global_store_dwordx4 v[8:9], v[26:29], off offset:1024 nt
	v_fma_f32 v8, -v31, v32, 1.0
	v_fmac_f32_e32 v32, v8, v32
	v_div_scale_f32 v8, vcc, 1.0, v30, 1.0
	v_mul_f32_e32 v9, v8, v32
	v_fma_f32 v26, -v31, v9, v8
	v_fmac_f32_e32 v9, v26, v32
	v_fma_f32 v8, -v31, v9, v8
	v_div_fmas_f32 v8, v8, v32, v9
	v_div_fixup_f32 v8, v8, v30, 1.0
	s_and_saveexec_b64 s[0:1], s[34:35]
	s_cbranch_execz .LBB0_41
	s_lshl_b64 s[4:5], s[44:45], 2
	s_add_u32 s4, s6, s4
	s_addc_u32 s5, s7, s5
	global_store_dword v49, v8, s[4:5]
	s_branch .LBB0_41

.LBB0_67:
	v_lshl_add_u64 v[0:1], s[42:43], 0, v[70:71]
	global_load_dwordx4 v[58:61], v[0:1], off offset:16 nt
	global_load_dwordx4 v[62:65], v[0:1], off nt
	global_load_dwordx4 v[50:53], v[0:1], off offset:2064 nt
	global_load_dwordx4 v[54:57], v[0:1], off offset:2048 nt
	v_lshl_add_u64 v[0:1], s[38:39], 0, v[70:71]
	global_load_dwordx4 v[40:43], v[0:1], off offset:16 nt
	global_load_dwordx4 v[44:47], v[0:1], off nt
	global_load_dwordx4 v[32:35], v[0:1], off offset:2064 nt
	global_load_dwordx4 v[36:39], v[0:1], off offset:2048 nt
	v_lshl_add_u64 v[0:1], s[46:47], 0, v[70:71]
	v_lshl_add_u64 v[4:5], s[44:45], 0, v[70:71]
	global_load_dwordx4 v[24:27], v[0:1], off offset:16 nt
	global_load_dwordx4 v[28:31], v[0:1], off nt
	global_load_dwordx4 v[16:19], v[0:1], off offset:2064 nt
	global_load_dwordx4 v[20:23], v[0:1], off offset:2048 nt
	global_load_dwordx4 v[8:11], v[4:5], off offset:16 nt
	global_load_dwordx4 v[12:15], v[4:5], off nt
	s_nop 0
	global_load_dwordx4 v[0:3], v[4:5], off offset:2064 nt
	s_nop 0
	global_load_dwordx4 v[4:7], v[4:5], off offset:2048 nt
	v_lshl_add_u64 v[94:95], s[40:41], 0, v[72:73]
	s_mov_b32 s0, 0x3fd00000
	v_add_co_u32_e32 v94, vcc, s0, v94
	s_mov_b32 s0, 0xf800000
	s_nop 0
	v_addc_co_u32_e32 v95, vcc, 0, v95, vcc
	s_waitcnt vmcnt(15)
	v_cvt_pk_bf16_f32 v92, v58, v59
	s_waitcnt vmcnt(14)
	v_mul_f32_e32 v89, v63, v63
	v_fmac_f32_e32 v89, v62, v62
	v_fmac_f32_e32 v89, v64, v64
	v_fmac_f32_e32 v89, v65, v65
	v_fmac_f32_e32 v89, v58, v58
	v_fmac_f32_e32 v89, v59, v59
	v_fmac_f32_e32 v89, v60, v60
	v_fmac_f32_e32 v89, v61, v61
	s_waitcnt vmcnt(12)
	v_fmac_f32_e32 v89, v54, v54
	v_fmac_f32_e32 v89, v55, v55
	v_fmac_f32_e32 v89, v56, v56
	v_fmac_f32_e32 v89, v57, v57
	v_fmac_f32_e32 v89, v50, v50
	v_fmac_f32_e32 v89, v51, v51
	v_cvt_pk_bf16_f32 v90, v62, v63
	v_cvt_pk_bf16_f32 v91, v64, v65
	v_cvt_pk_bf16_f32 v93, v60, v61
	v_fmac_f32_e32 v89, v52, v52
	global_store_dwordx4 v[94:95], v[90:93], off nt
	v_fmac_f32_e32 v89, v53, v53
	s_nop 0
	v_cvt_pk_bf16_f32 v90, v54, v55
	v_cvt_pk_bf16_f32 v91, v56, v57
	v_cvt_pk_bf16_f32 v92, v50, v51
	v_cvt_pk_bf16_f32 v93, v52, v53
	global_store_dwordx4 v[94:95], v[90:93], off offset:1024 nt
	ds_bpermute_b32 v90, v48, v89
	s_waitcnt lgkmcnt(0)
	v_add_f32_e32 v89, v89, v90
	ds_bpermute_b32 v90, v84, v89
	s_waitcnt lgkmcnt(0)
	v_add_f32_e32 v89, v89, v90
	ds_bpermute_b32 v90, v85, v89
	s_waitcnt lgkmcnt(0)
	v_add_f32_e32 v89, v89, v90
	ds_bpermute_b32 v90, v86, v89
	s_waitcnt lgkmcnt(0)
	v_add_f32_e32 v89, v89, v90
	ds_bpermute_b32 v90, v87, v89
	s_waitcnt lgkmcnt(0)
	v_add_f32_e32 v89, v89, v90
	ds_bpermute_b32 v90, v88, v89
	s_waitcnt lgkmcnt(0)
	v_add_f32_e32 v89, v89, v90
	v_fmamk_f32 v89, v89, 0x3a800000, v229
	v_cmp_gt_f32_e32 vcc, s0, v89
	v_mul_f32_e32 v90, 0x4f800000, v89
	s_nop 0
	v_cndmask_b32_e32 v89, v89, v90, vcc
	v_sqrt_f32_e32 v90, v89
	s_nop 0
	v_add_u32_e32 v91, -1, v90
	v_fma_f32 v92, -v91, v90, v89
	v_cmp_ge_f32_e64 s[36:37], 0, v92
	v_add_u32_e32 v92, 1, v90
	s_nop 0
	v_cndmask_b32_e64 v91, v90, v91, s[36:37]
	v_fma_f32 v90, -v92, v90, v89
	v_cmp_lt_f32_e64 s[36:37], 0, v90
	s_nop 1
	v_cndmask_b32_e64 v90, v91, v92, s[36:37]
	v_mul_f32_e32 v91, 0x37800000, v90
	v_cndmask_b32_e32 v90, v90, v91, vcc
	v_cmp_class_f32_e32 vcc, v89, v230
	s_nop 1
	v_cndmask_b32_e32 v89, v90, v89, vcc
	v_div_scale_f32 v90, s[0:1], v89, v89, 1.0
	v_rcp_f32_e32 v91, v90
	s_nop 0
	v_fma_f32 v92, -v90, v91, 1.0
	v_fmac_f32_e32 v91, v92, v91
	v_div_scale_f32 v92, vcc, 1.0, v89, 1.0
	v_mul_f32_e32 v93, v92, v91
	v_fma_f32 v94, -v90, v93, v92
	v_fmac_f32_e32 v93, v94, v91
	v_fma_f32 v90, -v90, v93, v92
	v_div_fmas_f32 v90, v90, v91, v93
	v_div_fixup_f32 v89, v90, v89, 1.0
	s_and_saveexec_b64 s[0:1], s[34:35]
	s_cbranch_execz .LBB0_69
	s_add_u32 s18, s40, s12
	s_addc_u32 s19, s41, s13
	global_store_dword v49, v89, s[18:19]
.LBB0_69:
	s_or_b64 exec, exec, s[0:1]
	v_mul_f32_e32 v89, 0x41800000, v89
	v_mul_f32_e32 v62, v62, v89
	v_mul_f32_e32 v63, v63, v89
	v_med3_f32 v90, v62, s11, v232
	v_med3_f32 v63, v63, s11, v232
	v_mov_b32_e32 v62, v49
	v_cvt_pk_fp8_f32 v62, v90, v63
	v_mul_f32_e32 v64, v64, v89
	v_mul_f32_e32 v63, v65, v89
	v_med3_f32 v64, v64, s11, v232
	v_med3_f32 v63, v63, s11, v232
	v_mul_f32_e32 v58, v58, v89
	v_mul_f32_e32 v59, v59, v89
	v_cvt_pk_fp8_f32 v62, v64, v63 op_sel:[0,0,1]
	v_mul_f32_e32 v60, v60, v89
	v_med3_f32 v58, v58, s11, v232
	v_med3_f32 v59, v59, s11, v232
	v_mov_b32_e32 v63, v49
	v_mul_f32_e32 v54, v54, v89
	v_mul_f32_e32 v55, v55, v89
	v_cvt_pk_fp8_f32 v63, v58, v59
	v_med3_f32 v59, v60, s11, v232
	v_mul_f32_e32 v56, v56, v89
	v_mul_f32_e32 v57, v57, v89
	v_med3_f32 v60, v54, s11, v232
	v_med3_f32 v55, v55, s11, v232
	v_mov_b32_e32 v54, v49
	v_cvt_pk_fp8_f32 v54, v60, v55
	v_med3_f32 v55, v56, s11, v232
	v_med3_f32 v56, v57, s11, v232
	s_waitcnt vmcnt(12)
	v_mul_f32_e32 v57, v45, v45
	v_fmac_f32_e32 v57, v44, v44
	v_fmac_f32_e32 v57, v46, v46
	v_fmac_f32_e32 v57, v47, v47
	v_fmac_f32_e32 v57, v40, v40
	v_fmac_f32_e32 v57, v41, v41
	v_fmac_f32_e32 v57, v42, v42
	v_fmac_f32_e32 v57, v43, v43
	s_waitcnt vmcnt(10)
	v_fmac_f32_e32 v57, v36, v36
	v_fmac_f32_e32 v57, v37, v37
	v_fmac_f32_e32 v57, v38, v38
	v_fmac_f32_e32 v57, v39, v39
	v_fmac_f32_e32 v57, v32, v32
	v_fmac_f32_e32 v57, v33, v33
	v_fmac_f32_e32 v57, v34, v34
	v_fmac_f32_e32 v57, v35, v35
	ds_bpermute_b32 v60, v48, v57
	v_cvt_pk_fp8_f32 v54, v55, v56 op_sel:[0,0,1]
	v_mul_f32_e32 v50, v50, v89
	v_mul_f32_e32 v51, v51, v89
	v_med3_f32 v50, v50, s11, v232
	s_waitcnt lgkmcnt(0)
	v_add_f32_e32 v56, v57, v60
	ds_bpermute_b32 v57, v84, v56
	v_med3_f32 v51, v51, s11, v232
	v_mov_b32_e32 v55, v49
	v_cvt_pk_fp8_f32 v55, v50, v51
	v_mul_f32_e32 v52, v52, v89
	s_waitcnt lgkmcnt(0)
	v_add_f32_e32 v50, v56, v57
	ds_bpermute_b32 v51, v85, v50
	v_mul_f32_e32 v53, v53, v89
	v_med3_f32 v52, v52, s11, v232
	v_med3_f32 v53, v53, s11, v232
	v_cvt_pk_fp8_f32 v55, v52, v53 op_sel:[0,0,1]
	s_waitcnt lgkmcnt(0)
	v_add_f32_e32 v52, v50, v51
	ds_bpermute_b32 v53, v86, v52
	v_mul_f32_e32 v58, v61, v89
	v_med3_f32 v58, v58, s11, v232
	v_cvt_pk_fp8_f32 v63, v59, v58 op_sel:[0,0,1]
	v_lshl_add_u64 v[58:59], s[40:41], 0, v[78:79]
	s_waitcnt lgkmcnt(0)
	v_add_f32_e32 v56, v52, v53
	ds_bpermute_b32 v57, v87, v56
	s_mov_b32 s0, 0x7100000
	v_add_co_u32_e32 v50, vcc, s0, v58
	s_mov_b32 s0, 0x3fd00000
	s_waitcnt lgkmcnt(0)
	v_add_f32_e32 v56, v56, v57
	ds_bpermute_b32 v57, v88, v56
	v_addc_co_u32_e32 v51, vcc, 0, v59, vcc
	global_store_dwordx2 v[50:51], v[62:63], off
	global_store_dwordx2 v[50:51], v[54:55], off offset:512
	v_lshl_add_u64 v[54:55], s[40:41], 0, v[82:83]
	v_add_co_u32_e32 v54, vcc, s0, v54
	s_waitcnt lgkmcnt(0)
	v_add_f32_e32 v56, v56, v57
	v_addc_co_u32_e32 v55, vcc, 0, v55, vcc
	v_fmamk_f32 v56, v56, 0x3a800000, v229
	s_mov_b32 s0, 0xf800000
	v_mul_f32_e32 v57, 0x4f800000, v56
	v_cmp_gt_f32_e32 vcc, s0, v56
	v_cvt_pk_bf16_f32 v50, v44, v45
	v_cvt_pk_bf16_f32 v51, v46, v47
	v_cndmask_b32_e32 v56, v56, v57, vcc
	v_sqrt_f32_e32 v57, v56
	v_cvt_pk_bf16_f32 v52, v40, v41
	v_cvt_pk_bf16_f32 v53, v42, v43
	global_store_dwordx4 v[54:55], v[50:53], off nt
	s_nop 1
	v_add_u32_e32 v52, -1, v57
	v_fma_f32 v53, -v52, v57, v56
	v_cmp_ge_f32_e64 s[36:37], 0, v53
	v_add_u32_e32 v53, 1, v57
	v_cvt_pk_bf16_f32 v50, v36, v37
	v_cndmask_b32_e64 v52, v57, v52, s[36:37]
	v_fma_f32 v57, -v53, v57, v56
	v_cmp_lt_f32_e64 s[36:37], 0, v57
	v_cvt_pk_bf16_f32 v51, v38, v39
	s_nop 0
	v_cndmask_b32_e64 v52, v52, v53, s[36:37]
	v_mul_f32_e32 v53, 0x37800000, v52
	v_cndmask_b32_e32 v52, v52, v53, vcc
	v_cmp_class_f32_e32 vcc, v56, v230
	v_cvt_pk_bf16_f32 v53, v34, v35
	s_nop 0
	v_cndmask_b32_e32 v56, v52, v56, vcc
	v_div_scale_f32 v57, s[0:1], v56, v56, 1.0
	v_rcp_f32_e32 v58, v57
	v_cvt_pk_bf16_f32 v52, v32, v33
	global_store_dwordx4 v[54:55], v[50:53], off offset:1024 nt
	s_nop 1
	v_fma_f32 v50, -v57, v58, 1.0
	v_fmac_f32_e32 v58, v50, v58
	v_div_scale_f32 v50, vcc, 1.0, v56, 1.0
	v_mul_f32_e32 v51, v50, v58
	v_fma_f32 v52, -v57, v51, v50
	v_fmac_f32_e32 v51, v52, v58
	v_fma_f32 v50, -v57, v51, v50
	v_div_fmas_f32 v50, v50, v58, v51
	v_div_fixup_f32 v50, v50, v56, 1.0
	s_and_saveexec_b64 s[0:1], s[34:35]
	s_cbranch_execz .LBB0_71
	s_add_u32 s18, s40, s9
	s_addc_u32 s19, s41, s10
	global_store_dword v49, v50, s[18:19]
.LBB0_71:
	s_or_b64 exec, exec, s[0:1]
	v_mul_f32_e32 v50, 0x41800000, v50
	v_mul_f32_e32 v44, v44, v50
	v_mul_f32_e32 v45, v45, v50
	v_med3_f32 v51, v44, s11, v232
	v_med3_f32 v45, v45, s11, v232
	v_mov_b32_e32 v44, v49
	v_cvt_pk_fp8_f32 v44, v51, v45
	v_mul_f32_e32 v46, v46, v50
	v_mul_f32_e32 v45, v47, v50
	v_med3_f32 v46, v46, s11, v232
	v_med3_f32 v45, v45, s11, v232
	v_mul_f32_e32 v40, v40, v50
	v_mul_f32_e32 v41, v41, v50
	v_cvt_pk_fp8_f32 v44, v46, v45 op_sel:[0,0,1]
	v_mul_f32_e32 v42, v42, v50
	v_med3_f32 v40, v40, s11, v232
	v_med3_f32 v41, v41, s11, v232
	v_mov_b32_e32 v45, v49
	v_mul_f32_e32 v36, v36, v50
	v_mul_f32_e32 v37, v37, v50
	v_cvt_pk_fp8_f32 v45, v40, v41
	v_med3_f32 v41, v42, s11, v232
	v_mul_f32_e32 v38, v38, v50
	v_mul_f32_e32 v39, v39, v50
	v_med3_f32 v42, v36, s11, v232
	v_med3_f32 v37, v37, s11, v232
	v_mov_b32_e32 v36, v49
	v_cvt_pk_fp8_f32 v36, v42, v37
	v_med3_f32 v37, v38, s11, v232
	v_med3_f32 v38, v39, s11, v232
	s_waitcnt vmcnt(12)
	v_mul_f32_e32 v39, v29, v29
	v_fmac_f32_e32 v39, v28, v28
	v_fmac_f32_e32 v39, v30, v30
	v_fmac_f32_e32 v39, v31, v31
	v_fmac_f32_e32 v39, v24, v24
	v_fmac_f32_e32 v39, v25, v25
	v_fmac_f32_e32 v39, v26, v26
	v_fmac_f32_e32 v39, v27, v27
	s_waitcnt vmcnt(10)
	v_fmac_f32_e32 v39, v20, v20
	v_fmac_f32_e32 v39, v21, v21
	v_fmac_f32_e32 v39, v22, v22
	v_fmac_f32_e32 v39, v23, v23
	v_fmac_f32_e32 v39, v16, v16
	v_fmac_f32_e32 v39, v17, v17
	v_fmac_f32_e32 v39, v18, v18
	v_fmac_f32_e32 v39, v19, v19
	ds_bpermute_b32 v42, v48, v39
	v_cvt_pk_fp8_f32 v36, v37, v38 op_sel:[0,0,1]
	v_mul_f32_e32 v32, v32, v50
	v_mul_f32_e32 v33, v33, v50
	v_med3_f32 v32, v32, s11, v232
	s_waitcnt lgkmcnt(0)
	v_add_f32_e32 v38, v39, v42
	ds_bpermute_b32 v39, v84, v38
	v_med3_f32 v33, v33, s11, v232
	v_mov_b32_e32 v37, v49
	v_cvt_pk_fp8_f32 v37, v32, v33
	v_mul_f32_e32 v34, v34, v50
	s_waitcnt lgkmcnt(0)
	v_add_f32_e32 v32, v38, v39
	ds_bpermute_b32 v33, v85, v32
	v_mul_f32_e32 v35, v35, v50
	v_med3_f32 v34, v34, s11, v232
	v_med3_f32 v35, v35, s11, v232
	v_cvt_pk_fp8_f32 v37, v34, v35 op_sel:[0,0,1]
	s_waitcnt lgkmcnt(0)
	v_add_f32_e32 v34, v32, v33
	ds_bpermute_b32 v35, v86, v34
	v_mul_f32_e32 v40, v43, v50
	v_med3_f32 v40, v40, s11, v232
	v_cvt_pk_fp8_f32 v45, v41, v40 op_sel:[0,0,1]
	v_lshl_add_u64 v[40:41], s[40:41], 0, v[80:81]
	s_waitcnt lgkmcnt(0)
	v_add_f32_e32 v38, v34, v35
	ds_bpermute_b32 v39, v87, v38
	s_mov_b32 s0, 0x7100000
	v_add_co_u32_e32 v32, vcc, s0, v40
	s_mov_b32 s0, 0x3fd00000
	s_waitcnt lgkmcnt(0)
	v_add_f32_e32 v38, v38, v39
	ds_bpermute_b32 v39, v88, v38
	v_addc_co_u32_e32 v33, vcc, 0, v41, vcc
	global_store_dwordx2 v[32:33], v[44:45], off
	global_store_dwordx2 v[32:33], v[36:37], off offset:512
	v_lshl_add_u64 v[36:37], s[40:41], 0, v[76:77]
	v_add_co_u32_e32 v36, vcc, s0, v36
	s_waitcnt lgkmcnt(0)
	v_add_f32_e32 v38, v38, v39
	v_addc_co_u32_e32 v37, vcc, 0, v37, vcc
	v_fmamk_f32 v38, v38, 0x3a800000, v229
	s_mov_b32 s0, 0xf800000
	v_mul_f32_e32 v39, 0x4f800000, v38
	v_cmp_gt_f32_e32 vcc, s0, v38
	v_cvt_pk_bf16_f32 v32, v28, v29
	v_cvt_pk_bf16_f32 v33, v30, v31
	v_cndmask_b32_e32 v38, v38, v39, vcc
	v_sqrt_f32_e32 v39, v38
	v_cvt_pk_bf16_f32 v34, v24, v25
	v_cvt_pk_bf16_f32 v35, v26, v27
	global_store_dwordx4 v[36:37], v[32:35], off nt
	s_nop 1
	v_add_u32_e32 v34, -1, v39
	v_fma_f32 v35, -v34, v39, v38
	v_cmp_ge_f32_e64 s[36:37], 0, v35
	v_add_u32_e32 v35, 1, v39
	v_cvt_pk_bf16_f32 v32, v20, v21
	v_cndmask_b32_e64 v34, v39, v34, s[36:37]
	v_fma_f32 v39, -v35, v39, v38
	v_cmp_lt_f32_e64 s[36:37], 0, v39
	v_cvt_pk_bf16_f32 v33, v22, v23
	s_nop 0
	v_cndmask_b32_e64 v34, v34, v35, s[36:37]
	v_mul_f32_e32 v35, 0x37800000, v34
	v_cndmask_b32_e32 v34, v34, v35, vcc
	v_cmp_class_f32_e32 vcc, v38, v230
	v_cvt_pk_bf16_f32 v35, v18, v19
	s_nop 0
	v_cndmask_b32_e32 v38, v34, v38, vcc
	v_div_scale_f32 v39, s[0:1], v38, v38, 1.0
	v_rcp_f32_e32 v40, v39
	v_cvt_pk_bf16_f32 v34, v16, v17
	global_store_dwordx4 v[36:37], v[32:35], off offset:1024 nt
	s_nop 1
	v_fma_f32 v32, -v39, v40, 1.0
	v_fmac_f32_e32 v40, v32, v40
	v_div_scale_f32 v32, vcc, 1.0, v38, 1.0
	v_mul_f32_e32 v33, v32, v40
	v_fma_f32 v34, -v39, v33, v32
	v_fmac_f32_e32 v33, v34, v40
	v_fma_f32 v32, -v39, v33, v32
	v_div_fmas_f32 v32, v32, v40, v33
	v_div_fixup_f32 v32, v32, v38, 1.0
	s_and_saveexec_b64 s[0:1], s[34:35]
	s_cbranch_execz .LBB0_73
	s_add_u32 s18, s40, s7
	s_addc_u32 s19, s41, s8
	global_store_dword v49, v32, s[18:19]
.LBB0_73:
	s_or_b64 exec, exec, s[0:1]
	v_mul_f32_e32 v32, 0x41800000, v32
	v_mul_f32_e32 v28, v28, v32
	v_mul_f32_e32 v29, v29, v32
	v_med3_f32 v33, v28, s11, v232
	v_med3_f32 v29, v29, s11, v232
	v_mov_b32_e32 v28, v49
	v_cvt_pk_fp8_f32 v28, v33, v29
	v_mul_f32_e32 v30, v30, v32
	v_mul_f32_e32 v29, v31, v32
	v_med3_f32 v30, v30, s11, v232
	v_med3_f32 v29, v29, s11, v232
	v_mul_f32_e32 v24, v24, v32
	v_mul_f32_e32 v25, v25, v32
	v_cvt_pk_fp8_f32 v28, v30, v29 op_sel:[0,0,1]
	v_mul_f32_e32 v26, v26, v32
	v_med3_f32 v24, v24, s11, v232
	v_med3_f32 v25, v25, s11, v232
	v_mov_b32_e32 v29, v49
	v_mul_f32_e32 v20, v20, v32
	v_mul_f32_e32 v21, v21, v32
	v_cvt_pk_fp8_f32 v29, v24, v25
	v_med3_f32 v25, v26, s11, v232
	v_mul_f32_e32 v22, v22, v32
	v_mul_f32_e32 v23, v23, v32
	v_med3_f32 v26, v20, s11, v232
	v_med3_f32 v21, v21, s11, v232
	v_mov_b32_e32 v20, v49
	v_cvt_pk_fp8_f32 v20, v26, v21
	v_med3_f32 v21, v22, s11, v232
	v_med3_f32 v22, v23, s11, v232
	s_waitcnt vmcnt(12)
	v_mul_f32_e32 v23, v13, v13
	v_fmac_f32_e32 v23, v12, v12
	v_fmac_f32_e32 v23, v14, v14
	v_fmac_f32_e32 v23, v15, v15
	v_fmac_f32_e32 v23, v8, v8
	v_fmac_f32_e32 v23, v9, v9
	v_fmac_f32_e32 v23, v10, v10
	v_fmac_f32_e32 v23, v11, v11
	s_waitcnt vmcnt(10)
	v_fmac_f32_e32 v23, v4, v4
	v_fmac_f32_e32 v23, v5, v5
	v_fmac_f32_e32 v23, v6, v6
	v_fmac_f32_e32 v23, v7, v7
	v_fmac_f32_e32 v23, v0, v0
	v_fmac_f32_e32 v23, v1, v1
	v_fmac_f32_e32 v23, v2, v2
	v_fmac_f32_e32 v23, v3, v3
	ds_bpermute_b32 v26, v48, v23
	v_cvt_pk_fp8_f32 v20, v21, v22 op_sel:[0,0,1]
	v_mul_f32_e32 v16, v16, v32
	v_mul_f32_e32 v17, v17, v32
	v_med3_f32 v16, v16, s11, v232
	s_waitcnt lgkmcnt(0)
	v_add_f32_e32 v22, v23, v26
	ds_bpermute_b32 v23, v84, v22
	v_med3_f32 v17, v17, s11, v232
	v_mov_b32_e32 v21, v49
	v_cvt_pk_fp8_f32 v21, v16, v17
	v_mul_f32_e32 v18, v18, v32
	s_waitcnt lgkmcnt(0)
	v_add_f32_e32 v16, v22, v23
	ds_bpermute_b32 v17, v85, v16
	v_mul_f32_e32 v19, v19, v32
	v_med3_f32 v18, v18, s11, v232
	v_med3_f32 v19, v19, s11, v232
	v_cvt_pk_fp8_f32 v21, v18, v19 op_sel:[0,0,1]
	s_waitcnt lgkmcnt(0)
	v_add_f32_e32 v18, v16, v17
	ds_bpermute_b32 v19, v86, v18
	v_mul_f32_e32 v24, v27, v32
	v_med3_f32 v24, v24, s11, v232
	v_cvt_pk_fp8_f32 v29, v25, v24 op_sel:[0,0,1]
	v_lshl_add_u64 v[24:25], s[40:41], 0, v[74:75]
	s_waitcnt lgkmcnt(0)
	v_add_f32_e32 v22, v18, v19
	ds_bpermute_b32 v23, v87, v22
	s_mov_b32 s0, 0x7100000
	v_add_co_u32_e32 v16, vcc, s0, v24
	s_mov_b32 s0, 0x3fd00000
	s_waitcnt lgkmcnt(0)
	v_add_f32_e32 v22, v22, v23
	ds_bpermute_b32 v23, v88, v22
	v_addc_co_u32_e32 v17, vcc, 0, v25, vcc
	global_store_dwordx2 v[16:17], v[28:29], off
	global_store_dwordx2 v[16:17], v[20:21], off offset:512
	v_lshl_add_u64 v[20:21], s[40:41], 0, v[68:69]
	v_add_co_u32_e32 v20, vcc, s0, v20
	s_waitcnt lgkmcnt(0)
	v_add_f32_e32 v22, v22, v23
	v_addc_co_u32_e32 v21, vcc, 0, v21, vcc
	v_fmamk_f32 v22, v22, 0x3a800000, v229
	s_mov_b32 s0, 0xf800000
	v_mul_f32_e32 v23, 0x4f800000, v22
	v_cmp_gt_f32_e32 vcc, s0, v22
	v_cvt_pk_bf16_f32 v16, v12, v13
	v_cvt_pk_bf16_f32 v17, v14, v15
	v_cndmask_b32_e32 v22, v22, v23, vcc
	v_sqrt_f32_e32 v23, v22
	v_cvt_pk_bf16_f32 v18, v8, v9
	v_cvt_pk_bf16_f32 v19, v10, v11
	global_store_dwordx4 v[20:21], v[16:19], off nt
	s_nop 1
	v_add_u32_e32 v18, -1, v23
	v_fma_f32 v19, -v18, v23, v22
	v_cmp_ge_f32_e64 s[36:37], 0, v19
	v_add_u32_e32 v19, 1, v23
	v_cvt_pk_bf16_f32 v16, v4, v5
	v_cndmask_b32_e64 v18, v23, v18, s[36:37]
	v_fma_f32 v23, -v19, v23, v22
	v_cmp_lt_f32_e64 s[36:37], 0, v23
	v_cvt_pk_bf16_f32 v17, v6, v7
	s_nop 0
	v_cndmask_b32_e64 v18, v18, v19, s[36:37]
	v_mul_f32_e32 v19, 0x37800000, v18
	v_cndmask_b32_e32 v18, v18, v19, vcc
	v_cmp_class_f32_e32 vcc, v22, v230
	v_cvt_pk_bf16_f32 v19, v2, v3
	s_nop 0
	v_cndmask_b32_e32 v22, v18, v22, vcc
	v_div_scale_f32 v23, s[0:1], v22, v22, 1.0
	v_rcp_f32_e32 v24, v23
	v_cvt_pk_bf16_f32 v18, v0, v1
	global_store_dwordx4 v[20:21], v[16:19], off offset:1024 nt
	s_nop 1
	v_fma_f32 v16, -v23, v24, 1.0
	v_fmac_f32_e32 v24, v16, v24
	v_div_scale_f32 v16, vcc, 1.0, v22, 1.0
	v_mul_f32_e32 v17, v16, v24
	v_fma_f32 v18, -v23, v17, v16
	v_fmac_f32_e32 v17, v18, v24
	v_fma_f32 v16, -v23, v17, v16
	v_div_fmas_f32 v16, v16, v24, v17
	v_div_fixup_f32 v16, v16, v22, 1.0
	s_and_saveexec_b64 s[0:1], s[34:35]
	s_cbranch_execz .LBB0_66
	s_add_u32 s18, s40, s5
	s_addc_u32 s19, s41, s6
	global_store_dword v49, v16, s[18:19]
	s_branch .LBB0_66
